# v23 + one static s_setprio 1 for waves 4-7 across the HGRN2 chunk loop
# speedup vs baseline: 1.0150x; 1.0025x over previous
.LBB0_354:
	v_add_u32_e32 v8, 0x200, v8
	s_movk_i32 s70, 0x1fff
	v_cmp_lt_u32_e32 vcc, s70, v8
	ds_write_b32 v7, v69
	s_or_b64 s[58:59], vcc, s[58:59]
	v_add_u32_e32 v7, 0x800, v7
	s_andn2_b64 exec, exec, s[58:59]
	s_cbranch_execnz .LBB0_354
	s_or_b64 exec, exec, s[58:59]
	s_waitcnt vmcnt(0)
	v_sub_f32_e32 v4, v4, v2
	v_mul_f32_e32 v2, 0x3fb8aa3b, v4
	s_mov_b32 s46, 0x3fb8aa3b
	v_fma_f32 v7, v4, s46, -v2
	v_rndne_f32_e32 v8, v2
	v_fmac_f32_e32 v7, 0x32a5705f, v4
	v_sub_f32_e32 v2, v2, v8
	v_add_f32_e32 v2, v2, v7
	v_cvt_i32_f32_e32 v7, v8
	v_exp_f32_e32 v2, v2
	v_sub_f32_e32 v3, v5, v3
	s_and_b64 s[58:59], s[40:41], exec
	v_readlane_b32 s58, v254, 15
	v_ldexp_f32 v7, v2, v7
	v_mul_f32_e32 v2, 0x3fb8aa3b, v3
	v_fma_f32 v5, v3, s46, -v2
	v_rndne_f32_e32 v8, v2
	v_fmac_f32_e32 v5, 0x32a5705f, v3
	v_sub_f32_e32 v2, v2, v8
	v_add_f32_e32 v2, v2, v5
	v_exp_f32_e32 v5, v2
	v_cvt_i32_f32_e32 v8, v8
	s_mov_b32 s46, 0xc2ce8ed0
	v_cmp_ngt_f32_e32 vcc, s46, v4
	s_mov_b32 s89, 0x42b17218
	v_ldexp_f32 v5, v5, v8
	v_cndmask_b32_e32 v7, 0, v7, vcc
	v_cmp_ngt_f32_e32 vcc, s46, v3
	v_readlane_b32 s46, v254, 26
	s_cselect_b32 s58, s58, s46
	v_cndmask_b32_e32 v5, 0, v5, vcc
	v_cmp_nlt_f32_e32 vcc, s89, v3
	s_mulk_i32 s58, 0x1c00
	v_readlane_b32 s46, v254, 27
	v_cndmask_b32_e32 v3, v215, v5, vcc
	v_or_b32_e32 v5, s58, v6
	s_cselect_b32 s58, s60, s46
	s_mulk_i32 s58, 0x1c00
	v_readlane_b32 s46, v254, 28
	v_readlane_b32 s47, v254, 29
	v_or_b32_e32 v8, s58, v6
	s_cselect_b32 s58, s46, s47
	s_mulk_i32 s58, 0x1c00
	v_readlane_b32 s46, v254, 30
	v_readlane_b32 s47, v254, 31
	v_or_b32_e32 v9, s58, v6
	s_cselect_b32 s58, s46, s47
	s_mulk_i32 s58, 0x1c00
	v_readlane_b32 s46, v254, 32
	v_readlane_b32 s47, v254, 33
	v_or_b32_e32 v10, s58, v6
	s_cselect_b32 s58, s46, s47
	s_mulk_i32 s58, 0x1c00
	v_readlane_b32 s46, v254, 34
	v_readlane_b32 s47, v254, 35
	v_or_b32_e32 v11, s58, v6
	s_cselect_b32 s58, s46, s47
	s_mulk_i32 s58, 0x1c00
	v_readlane_b32 s46, v254, 36
	v_readlane_b32 s47, v254, 37
	v_or_b32_e32 v12, s58, v6
	s_cselect_b32 s58, s46, s47
	s_mulk_i32 s58, 0x1c00
	v_readlane_b32 s46, v254, 38
	v_readlane_b32 s47, v254, 39
	v_or_b32_e32 v13, s58, v6
	s_cselect_b32 s58, s46, s47
	s_mulk_i32 s58, 0x1c00
	v_add_f32_e32 v3, 1.0, v3
	v_or_b32_e32 v6, s58, v6
	v_lshlrev_b32_e32 v50, 1, v6
	v_div_scale_f32 v6, s[58:59], v3, v3, 1.0
	s_movk_i32 s58, 0x1800
	s_cselect_b32 s70, s58, 0x2000
	s_mov_b32 s58, 0x16600000
	s_cselect_b32 s58, s58, 0x1a600000
	s_add_u32 s82, s66, s58
	s_addc_u32 s83, s67, 0
	s_lshl_b32 s58, s5, 7
	s_and_b32 s88, s58, 0xfffff800
	s_and_b64 s[58:59], s[40:41], exec
	s_cselect_b32 s58, 0, 0x7c0
	s_or_b32 s58, s58, s88
	s_mul_hi_i32 s59, s58, 0x3800
	s_mulk_i32 s58, 0x3800
	s_add_u32 s86, s55, s58
	s_addc_u32 s87, s73, s59
	s_add_u32 s58, s86, s70
	s_addc_u32 s59, s87, 0
	s_add_u32 s84, s86, 0x1000
	s_addc_u32 s85, s87, 0
	v_lshlrev_b32_e32 v68, 1, v5
	s_add_u32 s86, s86, 0x2800
	v_lshlrev_b32_e32 v52, 1, v8
	v_lshlrev_b32_e32 v54, 1, v9
	v_lshlrev_b32_e32 v56, 1, v10
	v_lshlrev_b32_e32 v58, 1, v11
	v_lshlrev_b32_e32 v60, 1, v12
	v_lshlrev_b32_e32 v62, 1, v13
	s_addc_u32 s87, s87, 0
	global_load_dword v87, v68, s[58:59]
	global_load_dword v89, v68, s[84:85]
	global_load_dword v91, v68, s[86:87]
	global_load_dword v93, v52, s[58:59]
	global_load_dword v97, v52, s[84:85]
	global_load_dword v107, v52, s[86:87]
	global_load_dword v147, v54, s[84:85]
	global_load_dword v148, v54, s[86:87]
	global_load_dword v146, v54, s[58:59]
	global_load_dword v149, v56, s[58:59]
	global_load_dword v150, v56, s[84:85]
	global_load_dword v151, v56, s[86:87]
	global_load_dword v152, v58, s[58:59]
	global_load_dword v153, v58, s[84:85]
	global_load_dword v154, v58, s[86:87]
	global_load_dword v157, v60, s[86:87]
	global_load_dword v155, v60, s[58:59]
	global_load_dword v156, v60, s[84:85]
	global_load_dword v158, v62, s[58:59]
	global_load_dword v159, v62, s[84:85]
	global_load_dword v160, v62, s[86:87]
	global_load_dword v161, v50, s[58:59]
	global_load_dword v164, v50, s[84:85]
	global_load_dword v165, v50, s[86:87]
	v_rcp_f32_e32 v14, v6
	v_cmp_nlt_f32_e32 vcc, s89, v4
	v_readlane_b32 s46, v254, 40
	s_waitcnt lgkmcnt(0)
	v_fma_f32 v5, -v6, v14, 1.0
	v_cndmask_b32_e32 v4, v215, v7, vcc
	v_fmac_f32_e32 v14, v5, v14
	v_div_scale_f32 v5, vcc, 1.0, v3, 1.0
	v_mul_f32_e32 v7, v5, v14
	v_fma_f32 v8, -v6, v7, v5
	v_fmac_f32_e32 v7, v8, v14
	v_fma_f32 v5, -v6, v7, v5
	v_add_f32_e32 v4, 1.0, v4
	v_div_fmas_f32 v5, v5, v14, v7
	v_div_fixup_f32 v65, v5, v3, 1.0
	v_div_scale_f32 v3, s[58:59], v4, v4, 1.0
	v_rcp_f32_e32 v5, v3
	v_or_b32_e32 v6, s61, v189
	v_lshlrev_b32_e32 v6, 1, v6
	s_barrier
	v_fma_f32 v7, -v3, v5, 1.0
	v_fmac_f32_e32 v5, v7, v5
	v_div_scale_f32 v7, vcc, 1.0, v4, 1.0
	v_mul_f32_e32 v8, v7, v5
	v_fma_f32 v9, -v3, v8, v7
	v_fmac_f32_e32 v8, v9, v5
	v_fma_f32 v3, -v3, v8, v7
	v_div_fmas_f32 v3, v3, v5, v8
	v_div_fixup_f32 v64, v3, v4, 1.0
	v_cndmask_b32_e64 v3, v188, v187, s[40:41]
	v_lshlrev_b32_e32 v3, 11, v3
	v_mov_b32_e32 v2, 0
	v_or3_b32 v4, v6, s46, v3
	v_mov_b32_e32 v5, v69
	s_mov_b32 s89, 0
	v_pk_add_f32 v[108:109], v[64:65], 1.0 op_sel_hi:[1,0] neg_lo:[1,0] neg_hi:[1,0]
	v_mov_b32_e32 v53, v69
	v_mov_b32_e32 v55, v69
	v_mov_b32_e32 v57, v69
	v_mov_b32_e32 v59, v69
	v_mov_b32_e32 v61, v69
	v_mov_b32_e32 v63, v69
	v_mov_b32_e32 v51, v69
	v_lshl_add_u64 v[110:111], s[82:83], 0, v[4:5]
	s_movk_i32 s90, 0x780
	s_mov_b32 s91, 0
	v_mov_b32_e32 v3, v2
	v_mov_b32_e32 v4, v2
	v_mov_b32_e32 v5, v2
	v_mov_b32_e32 v6, v2
	v_mov_b32_e32 v7, v2
	v_mov_b32_e32 v8, v2
	v_mov_b32_e32 v9, v2
	v_mov_b32_e32 v10, v2
	v_mov_b32_e32 v11, v2
	v_mov_b32_e32 v12, v2
	v_mov_b32_e32 v13, v2
	v_mov_b32_e32 v14, v2
	v_mov_b32_e32 v15, v2
	v_mov_b32_e32 v16, v2
	v_mov_b32_e32 v17, v2
	v_mov_b32_e32 v18, v2
	v_mov_b32_e32 v19, v2
	v_mov_b32_e32 v20, v2
	v_mov_b32_e32 v21, v2
	v_mov_b32_e32 v22, v2
	v_mov_b32_e32 v23, v2
	v_mov_b32_e32 v24, v2
	v_mov_b32_e32 v25, v2
	v_mov_b32_e32 v26, v2
	v_mov_b32_e32 v27, v2
	v_mov_b32_e32 v28, v2
	v_mov_b32_e32 v29, v2
	v_mov_b32_e32 v30, v2
	v_mov_b32_e32 v31, v2
	v_mov_b32_e32 v32, v2
	v_mov_b32_e32 v33, v2
	s_cmp_ge_u32 s57, 4
	s_cbranch_scc0 .Lhg_prio_done
	s_setprio 1
.Lhg_prio_done:
	s_branch .LBB0_357

.LBB0_367:
	s_setprio 0
	s_lshr_b32 s0, s56, 31
	s_add_i32 s0, s56, s0
	s_ashr_i32 s0, s0, 1
	v_readlane_b32 s78, v254, 5
	s_cmp_ge_i32 s78, s0
	v_readlane_b32 s79, v254, 8
	v_readlane_b32 s60, v254, 4
	s_cbranch_scc0 .LBB0_409
	s_sub_i32 s10, s78, s0
	s_cmpk_gt_u32 s10, 0x37f
	s_waitcnt vmcnt(0) lgkmcnt(0)
	s_barrier
	s_cbranch_scc1 .LBB0_409
	s_sub_i32 s0, s56, s0
	s_abs_i32 s2, s0
	v_cvt_f32_u32_e32 v2, s2
	s_sub_i32 s3, s0, s10
	s_add_i32 s4, s3, 0x37f
	s_sub_i32 s3, 0xfffffc81, s3
	v_rcp_iflag_f32_e32 v2, v2
	s_xor_b32 s6, s4, s0
	s_sub_i32 s5, 0, s2
	s_max_i32 s3, s4, s3
	v_mul_f32_e32 v2, 0x4f7ffffe, v2
	v_cvt_u32_f32_e32 v2, v2
	s_ashr_i32 s4, s6, 31
	s_add_i32 s1, s10, 0x2000
	v_readfirstlane_b32 s6, v2
	s_mul_i32 s5, s5, s6
	s_mul_hi_u32 s5, s6, s5
	s_add_i32 s6, s6, s5
	s_mul_hi_u32 s5, s3, s6
	s_mul_i32 s6, s5, s2
	s_sub_i32 s3, s3, s6
	s_add_i32 s7, s5, 1
	s_sub_i32 s6, s3, s2
	s_cmp_ge_u32 s3, s2
	s_cselect_b32 s5, s7, s5
	s_cselect_b32 s3, s6, s3
	s_add_i32 s6, s5, 1
	s_cmp_ge_u32 s3, s2
	s_cselect_b32 s2, s6, s5
	s_xor_b32 s2, s2, s4
	s_sub_i32 s18, s2, s4
	s_mov_b32 s18, 7
	s_movk_i32 s0, 0xff80
	s_lshl_b32 s12, s18, 2
	s_add_i32 s13, s12, -1
	s_cmp_gt_i32 s18, 0
	s_cselect_b64 s[2:3], -1, 0
	s_and_b64 s[4:5], s[2:3], exec
	s_cselect_b32 s11, 0, s13
	s_ashr_i32 s4, s11, 2
	s_mul_i32 s9, s4, s0
	s_add_i32 s9, s9, s1
	s_cmpk_gt_i32 s9, 0x1fff
	s_mov_b32 s5, 0
	s_cbranch_scc0 .LBB0_371
	s_add_i32 s4, s9, 0xffffe000
	s_lshr_b32 s4, s4, 7
	s_lshl_b64 s[4:5], s[4:5], 24
	v_readlane_b32 s34, v254, 13
	v_readlane_b32 s35, v254, 14
	s_add_u32 s6, s34, s4
	s_addc_u32 s7, s35, s5
	s_lshl_b32 s4, s9, 4
	s_and_b32 s19, s4, 0x780
	s_lshl_b32 s4, s9, 8
	v_readlane_b32 s30, v254, 11
	s_and_b32 s8, s4, 0x700
	v_readlane_b32 s31, v254, 12
	s_mov_b64 s[4:5], 0x800
	s_cbranch_execz .LBB0_372
	s_branch .LBB0_373
